# M7: M2 + s_setprio 3 on the baseline K2's four adj-loader waves
# baseline (speedup 1.0000x reference)
.LBB1_65:
	s_andn2_saveexec_b64 s[4:5], s[12:13]
	s_cbranch_execz .LBB1_103
	s_setprio 3
	s_load_dwordx2 s[4:5], s[0:1], 0x0
	s_load_dwordx2 s[6:7], s[0:1], 0x10
	s_mul_i32 s0, s28, 0xffffffd0
	s_add_i32 s9, s0, s3
	s_lshr_b32 s0, s29, 31
	s_ashr_i32 s12, s29, 9
	s_add_i32 s12, s12, s0
	s_mul_i32 s0, s12, 0xffffffd0
	s_add_i32 s0, s0, s28
	v_add_u32_e32 v103, -8, v98
	v_lshrrev_b32_e32 v1, 4, v102
	s_mul_i32 s1, s12, 0xc00
	s_lshl_b32 s0, s0, 6
	v_lshl_or_b32 v1, v103, 4, v1
	v_lshlrev_b32_e32 v2, 2, v0
	s_add_i32 s0, s0, s1
	v_and_b32_e32 v4, 60, v2
	v_add_u32_e32 v2, s0, v1
	s_movk_i32 s8, 0x3000
	s_waitcnt vmcnt(6) lgkmcnt(0)
	v_mov_b64_e32 v[82:83], s[4:5]
	v_mad_i64_i32 v[2:3], s[0:1], v2, s8, v[82:83]
	s_lshl_b32 s0, s9, 6
	s_ashr_i32 s1, s0, 31
	s_add_i32 s13, s3, 1
	v_lshl_add_u64 v[2:3], s[0:1], 2, v[2:3]
	s_mul_hi_i32 s0, s13, 0x2aaaaaab
	s_lshr_b32 s1, s0, 31
	s_ashr_i32 s0, s0, 3
	s_add_i32 s14, s0, s1
	s_mul_i32 s0, s14, 0xffffffd0
	s_add_i32 s9, s0, s13
	s_mul_hi_i32 s0, s13, 0x38e38e39
	s_lshr_b32 s1, s0, 31
	s_ashr_i32 s0, s0, 9
	s_add_i32 s15, s0, s1
	s_mul_i32 s0, s15, 0xffffffd0
	s_add_i32 s0, s0, s14
	s_mul_i32 s1, s15, 0xc00
	s_lshl_b32 s0, s0, 6
	v_mov_b32_e32 v125, 0
	v_lshlrev_b32_e32 v124, 2, v4
	s_add_i32 s0, s0, s1
	s_waitcnt vmcnt(2)
	v_lshl_add_u64 v[90:91], v[2:3], 0, v[124:125]
	v_add_u32_e32 v2, s0, v1
	v_mad_i64_i32 v[2:3], s[0:1], v2, s8, v[82:83]
	s_lshl_b32 s0, s9, 6
	s_ashr_i32 s1, s0, 31
	v_lshl_add_u64 v[2:3], s[0:1], 2, v[2:3]
	s_waitcnt vmcnt(1)
	v_lshl_add_u64 v[78:79], v[2:3], 0, v[124:125]
	s_mov_b32 s9, 0xc000
	v_add_co_u32_e32 v2, vcc, s9, v78
	s_mul_i32 s14, s14, 48
	s_nop 0
	v_addc_co_u32_e32 v3, vcc, 0, v79, vcc
	s_mov_b32 s10, 0x18000
	s_sub_i32 s0, s13, s14
	v_add_co_u32_e32 v4, vcc, s10, v78
	s_mul_i32 s1, s15, 0xc0
	s_lshl_b32 s0, s0, 2
	v_addc_co_u32_e32 v5, vcc, 0, v79, vcc
	s_mov_b32 s11, 0x24000
	s_add_i32 s0, s1, s0
	v_mov_b32_e32 v123, v125
	global_load_dwordx4 v[34:37], v[2:3], off nt
	global_load_dwordx4 v[26:29], v[4:5], off nt
	v_add_co_u32_e32 v2, vcc, s11, v78
	s_ashr_i32 s1, s0, 31
	v_lshl_add_u64 v[126:127], s[6:7], 0, v[122:123]
	v_addc_co_u32_e32 v3, vcc, 0, v79, vcc
	s_lshl_b64 s[0:1], s[0:1], 8
	s_add_i32 s13, s3, 2
	global_load_dwordx4 v[22:25], v[2:3], off nt
	v_lshl_add_u64 v[2:3], v[126:127], 0, s[0:1]
	s_mul_hi_i32 s0, s13, 0x2aaaaaab
	s_lshr_b32 s1, s0, 31
	s_ashr_i32 s0, s0, 3
	s_add_i32 s14, s0, s1
	s_mul_i32 s0, s14, 0xffffffd0
	s_add_i32 s15, s0, s13
	s_mul_hi_i32 s0, s13, 0x38e38e39
	s_lshr_b32 s1, s0, 31
	s_ashr_i32 s0, s0, 9
	s_add_i32 s16, s0, s1
	s_mul_i32 s0, s16, 0xffffffd0
	s_add_i32 s0, s0, s14
	s_mul_i32 s1, s16, 0xc00
	s_lshl_b32 s0, s0, 6
	s_add_i32 s0, s0, s1
	global_load_dwordx4 v[14:17], v[2:3], off
	v_add_u32_e32 v2, s0, v1
	v_mad_i64_i32 v[2:3], s[0:1], v2, s8, v[82:83]
	s_lshl_b32 s0, s15, 6
	s_ashr_i32 s1, s0, 31
	v_lshl_add_u64 v[2:3], s[0:1], 2, v[2:3]
	v_lshl_add_u64 v[2:3], v[2:3], 0, v[124:125]
	v_add_co_u32_e32 v4, vcc, s9, v2
	s_mul_i32 s14, s14, 48
	s_nop 0
	v_addc_co_u32_e32 v5, vcc, 0, v3, vcc
	s_sub_i32 s0, s13, s14
	global_load_dwordx4 v[30:33], v[2:3], off nt
	global_load_dwordx4 v[18:21], v[4:5], off nt
	v_add_co_u32_e32 v4, vcc, s10, v2
	s_mul_i32 s1, s16, 0xc0
	s_lshl_b32 s0, s0, 2
	v_addc_co_u32_e32 v5, vcc, 0, v3, vcc
	s_add_i32 s0, s1, s0
	v_add_co_u32_e32 v2, vcc, s11, v2
	s_ashr_i32 s1, s0, 31
	s_nop 0
	v_addc_co_u32_e32 v3, vcc, 0, v3, vcc
	s_lshl_b64 s[0:1], s[0:1], 8
	s_add_i32 s13, s3, 3
	global_load_dwordx4 v[10:13], v[4:5], off nt
	global_load_dwordx4 v[6:9], v[2:3], off nt
	v_lshl_add_u64 v[2:3], v[126:127], 0, s[0:1]
	s_mul_hi_i32 s0, s13, 0x2aaaaaab
	s_lshr_b32 s1, s0, 31
	s_ashr_i32 s0, s0, 3
	s_add_i32 s14, s0, s1
	s_mul_i32 s0, s14, 0xffffffd0
	s_add_i32 s15, s0, s13
	s_mul_hi_i32 s0, s13, 0x38e38e39
	s_lshr_b32 s1, s0, 31
	s_ashr_i32 s0, s0, 9
	s_add_i32 s16, s0, s1
	s_mul_i32 s0, s16, 0xffffffd0
	s_add_i32 s0, s0, s14
	s_mul_i32 s1, s16, 0xc00
	s_lshl_b32 s0, s0, 6
	s_add_i32 s0, s0, s1
	v_add_u32_e32 v38, s0, v1
	v_mad_i64_i32 v[38:39], s[0:1], v38, s8, v[82:83]
	s_lshl_b32 s0, s15, 6
	s_ashr_i32 s1, s0, 31
	v_lshl_add_u64 v[38:39], s[0:1], 2, v[38:39]
	v_lshl_add_u64 v[38:39], v[38:39], 0, v[124:125]
	s_mul_i32 s14, s14, 48
	v_add_co_u32_e32 v40, vcc, s9, v38
	s_sub_i32 s0, s13, s14
	s_nop 0
	v_addc_co_u32_e32 v41, vcc, 0, v39, vcc
	s_mul_i32 s1, s16, 0xc0
	s_lshl_b32 s0, s0, 2
	v_add_co_u32_e32 v50, vcc, s10, v38
	s_add_i32 s0, s1, s0
	s_nop 0
	v_addc_co_u32_e32 v51, vcc, 0, v39, vcc
	s_ashr_i32 s1, s0, 31
	v_add_co_u32_e32 v52, vcc, s11, v38
	s_lshl_b64 s[0:1], s[0:1], 8
	s_add_i32 s13, s3, 4
	global_load_dwordx4 v[2:5], v[2:3], off
	s_nop 0
	global_load_dwordx4 v[54:57], v[38:39], off nt
	global_load_dwordx4 v[42:45], v[40:41], off nt
	v_addc_co_u32_e32 v53, vcc, 0, v39, vcc
	global_load_dwordx4 v[46:49], v[50:51], off nt
	global_load_dwordx4 v[38:41], v[52:53], off nt
	v_lshl_add_u64 v[50:51], v[126:127], 0, s[0:1]
	s_mul_hi_i32 s0, s13, 0x2aaaaaab
	s_lshr_b32 s1, s0, 31
	s_ashr_i32 s0, s0, 3
	s_add_i32 s14, s0, s1
	s_mul_i32 s0, s14, 0xffffffd0
	s_add_i32 s15, s0, s13
	s_mul_hi_i32 s0, s13, 0x38e38e39
	s_lshr_b32 s1, s0, 31
	s_ashr_i32 s0, s0, 9
	s_add_i32 s16, s0, s1
	s_mul_i32 s0, s16, 0xffffffd0
	s_add_i32 s0, s0, s14
	s_mul_i32 s1, s16, 0xc00
	s_lshl_b32 s0, s0, 6
	s_add_i32 s0, s0, s1
	v_add_u32_e32 v58, s0, v1
	v_mad_i64_i32 v[58:59], s[0:1], v58, s8, v[82:83]
	s_lshl_b32 s0, s15, 6
	s_ashr_i32 s1, s0, 31
	s_mul_i32 s14, s14, 48
	v_lshl_add_u64 v[58:59], s[0:1], 2, v[58:59]
	s_sub_i32 s0, s13, s14
	s_mul_i32 s1, s16, 0xc0
	s_lshl_b32 s0, s0, 2
	s_add_i32 s0, s1, s0
	s_ashr_i32 s1, s0, 31
	s_lshl_b64 s[0:1], s[0:1], 8
	s_add_i32 s13, s3, 5
	v_lshl_add_u64 v[70:71], v[126:127], 0, s[0:1]
	s_mul_hi_i32 s0, s13, 0x2aaaaaab
	s_lshr_b32 s1, s0, 31
	s_ashr_i32 s0, s0, 3
	s_add_i32 s14, s0, s1
	s_mul_i32 s0, s14, 0xffffffd0
	s_add_i32 s15, s0, s13
	s_mul_hi_i32 s0, s13, 0x38e38e39
	s_lshr_b32 s1, s0, 31
	s_ashr_i32 s0, s0, 9
	s_add_i32 s16, s0, s1
	v_lshl_add_u64 v[58:59], v[58:59], 0, v[124:125]
	s_mul_i32 s0, s16, 0xffffffd0
	v_add_co_u32_e32 v60, vcc, s9, v58
	s_add_i32 s0, s0, s14
	s_nop 0
	v_addc_co_u32_e32 v61, vcc, 0, v59, vcc
	s_mul_i32 s1, s16, 0xc00
	s_lshl_b32 s0, s0, 6
	global_load_dwordx4 v[50:53], v[50:51], off
	s_nop 0
	global_load_dwordx4 v[74:77], v[58:59], off nt
	global_load_dwordx4 v[62:65], v[60:61], off nt
	v_add_co_u32_e32 v60, vcc, s10, v58
	s_add_i32 s0, s0, s1
	s_nop 0
	v_addc_co_u32_e32 v61, vcc, 0, v59, vcc
	v_add_u32_e32 v84, s0, v1
	v_add_co_u32_e32 v58, vcc, s11, v58
	v_mad_i64_i32 v[82:83], s[0:1], v84, s8, v[82:83]
	s_nop 0
	v_addc_co_u32_e32 v59, vcc, 0, v59, vcc
	s_lshl_b32 s0, s15, 6
	global_load_dwordx4 v[66:69], v[60:61], off nt
	s_nop 0
	global_load_dwordx4 v[58:61], v[58:59], off nt
	s_ashr_i32 s1, s0, 31
	global_load_dwordx4 v[70:73], v[70:71], off
	s_nop 0
	global_load_dwordx4 v[78:81], v[78:79], off nt
	s_nop 0
	global_load_dwordx4 v[104:107], v[90:91], off nt
	v_lshl_add_u64 v[82:83], s[0:1], 2, v[82:83]
	v_lshl_add_u64 v[92:93], v[82:83], 0, v[124:125]
	v_add_co_u32_e32 v82, vcc, s9, v90
	s_mul_i32 s14, s14, 48
	s_nop 0
	v_addc_co_u32_e32 v83, vcc, 0, v91, vcc
	global_load_dwordx4 v[108:111], v[82:83], off nt
	v_add_co_u32_e32 v82, vcc, s9, v92
	s_sub_i32 s0, s13, s14
	s_nop 0
	v_addc_co_u32_e32 v83, vcc, 0, v93, vcc
	v_add_co_u32_e32 v94, vcc, s10, v90
	global_load_dwordx4 v[86:89], v[92:93], off nt
	s_nop 0
	global_load_dwordx4 v[82:85], v[82:83], off nt
	v_addc_co_u32_e32 v95, vcc, 0, v91, vcc
	global_load_dwordx4 v[116:119], v[94:95], off nt
	v_add_co_u32_e32 v94, vcc, s10, v92
	s_mul_i32 s1, s16, 0xc0
	s_nop 0
	v_addc_co_u32_e32 v95, vcc, 0, v93, vcc
	v_add_co_u32_e32 v90, vcc, s11, v90
	s_lshl_b32 s0, s0, 2
	s_nop 0
	v_addc_co_u32_e32 v91, vcc, 0, v91, vcc
	global_load_dwordx4 v[130:133], v[90:91], off nt
	s_add_i32 s0, s1, s0
	v_add_co_u32_e32 v90, vcc, s11, v92
	s_ashr_i32 s1, s0, 31
	s_nop 0
	v_addc_co_u32_e32 v91, vcc, 0, v93, vcc
	s_lshl_b64 s[0:1], s[0:1], 8
	global_load_dwordx4 v[98:101], v[94:95], off nt
	s_nop 0
	global_load_dwordx4 v[90:93], v[90:91], off nt
	v_lshl_add_u64 v[94:95], v[126:127], 0, s[0:1]
	global_load_dwordx4 v[94:97], v[94:95], off
	v_bfrev_b32_e32 v0, v0
	v_lshrrev_b32_e32 v0, 27, v0
	v_lshlrev_b32_e32 v114, 3, v102
	v_and_b32_e32 v0, 24, v0
	s_movk_i32 s0, 0x60
	v_and_or_b32 v128, v114, s0, v0
	v_mov_b32_e32 v0, 0xffff
	v_mov_b32_e32 v123, 0xffff0000
	s_movk_i32 s0, 0x90
	s_waitcnt vmcnt(8)
	v_cmp_lt_i32_e32 vcc, 0, v106
	s_nop 1
	v_cndmask_b32_e32 v102, 0, v0, vcc
	v_cmp_lt_i32_e32 vcc, 0, v104
	s_nop 1
	v_cndmask_b32_e32 v104, 0, v0, vcc
	v_cmp_lt_i32_e32 vcc, 0, v107
	s_nop 1
	v_cndmask_b32_e32 v106, 0, v123, vcc
	v_cmp_lt_i32_e32 vcc, 0, v105
	v_or_b32_e32 v105, v106, v102
	v_mad_i32_i24 v102, v1, s0, v128
	v_cndmask_b32_e32 v107, 0, v123, vcc
	s_waitcnt vmcnt(7)
	v_cmp_lt_i32_e32 vcc, 0, v110
	v_or_b32_e32 v104, v107, v104
	s_nop 0
	v_cndmask_b32_e32 v106, 0, v0, vcc
	v_cmp_lt_i32_e32 vcc, 0, v108
	s_nop 1
	v_cndmask_b32_e32 v108, 0, v0, vcc
	v_cmp_lt_i32_e32 vcc, 0, v111
	s_nop 1
	v_cndmask_b32_e32 v107, 0, v123, vcc
	v_cmp_lt_i32_e32 vcc, 0, v109
	v_or_b32_e32 v107, v107, v106
	s_nop 0
	v_cndmask_b32_e32 v109, 0, v123, vcc
	v_or_b32_e32 v106, v109, v108
	s_waitcnt vmcnt(4)
	v_cmp_lt_i32_e32 vcc, 0, v118
	ds_write2_b64 v102, v[104:105], v[106:107] offset1:72
	s_nop 0
	v_cndmask_b32_e32 v104, 0, v0, vcc
	v_cmp_lt_i32_e32 vcc, 0, v116
	s_nop 1
	v_cndmask_b32_e32 v106, 0, v0, vcc
	v_cmp_lt_i32_e32 vcc, 0, v119
	s_nop 1
	v_cndmask_b32_e32 v105, 0, v123, vcc
	v_cmp_lt_i32_e32 vcc, 0, v117
	v_or_b32_e32 v105, v105, v104
	s_nop 0
	v_cndmask_b32_e32 v107, 0, v123, vcc
	s_waitcnt vmcnt(3)
	v_cmp_lt_i32_e32 vcc, 0, v132
	v_or_b32_e32 v104, v107, v106
	s_nop 0
	v_cndmask_b32_e32 v106, 0, v0, vcc
	v_cmp_lt_i32_e32 vcc, 0, v130
	s_nop 1
	v_cndmask_b32_e32 v108, 0, v0, vcc
	v_cmp_lt_i32_e32 vcc, 0, v133
	s_nop 1
	v_cndmask_b32_e32 v107, 0, v123, vcc
	v_cmp_lt_i32_e32 vcc, 0, v131
	v_or_b32_e32 v107, v107, v106
	s_nop 0
	v_cndmask_b32_e32 v109, 0, v123, vcc
	v_or_b32_e32 v106, v109, v108
	v_cmp_eq_u32_e32 vcc, 0, v103
	ds_write2_b64 v102, v[104:105], v[106:107] offset0:144 offset1:216
	s_and_saveexec_b64 s[0:1], vcc
	s_cbranch_execz .LBB1_68
	s_lshr_b32 s13, s26, 3
	s_add_i32 s13, s13, s27
	s_mul_i32 s13, s13, 48
	s_sub_i32 s13, s3, s13
	s_mulk_i32 s12, 0xc0
	s_lshl_b32 s13, s13, 2
	s_add_i32 s12, s12, s13
	s_ashr_i32 s13, s12, 31
	s_lshl_b64 s[12:13], s[12:13], 8
	v_lshl_add_u64 v[102:103], v[126:127], 0, s[12:13]
	global_load_dwordx4 v[102:105], v[102:103], off
	s_waitcnt vmcnt(0)
	ds_write_b128 v122, v[102:105] offset:18432
